# baseline (speedup 1.0000x reference)
.Lk2f_i1:
	s_mov_b64 exec, s[6:7]
	s_movk_i32 s5, 0x80
	v_cmp_gt_u32_e32 vcc, s5, v0
	v_lshlrev_b32_e32 v3, 2, v0
	v_mov_b32_e32 v8, 0
	s_and_saveexec_b64 s[6:7], vcc
	s_cbranch_execz .Lk2f_i2
	ds_write_b32 v3, v8 offset:18688
	ds_write_b32 v3, v8 offset:38832

.Lk2f_l6:
	s_waitcnt lgkmcnt(0)
	s_barrier
	s_cmp_lt_u32 s4, 4
	s_cbranch_scc0 .Lk2f_b2
	s_waitcnt vmcnt(0)
	v_mov_b32_e32 v9, 1
	s_mov_b32 s43, 0xc350
	v_mov_b32_e32 v62, 20144
	v_cmp_lt_i32_e32 vcc, 0, v24
	s_mov_b64 exec, vcc
	s_cbranch_execz .Lk2f_atd
	v_and_b32_e32 v60, 0x1ffff, v26
	v_cmp_le_u32_e32 vcc, s43, v60
	v_ashrrev_i32_e32 v42, 17, v26
	v_lshlrev_b32_e32 v42, 2, v42
	v_cndmask_b32_e32 v61, 0, v62, vcc
	v_add_u32_e32 v42, v42, v61
	ds_add_rtn_u32 v44, v42, v9 offset:18688
	v_cmp_lt_i32_e32 vcc, 1, v24
	s_mov_b64 exec, vcc
	s_cbranch_execz .Lk2f_atd
	v_and_b32_e32 v60, 0x1ffff, v27
	v_cmp_le_u32_e32 vcc, s43, v60
	v_ashrrev_i32_e32 v43, 17, v27
	v_lshlrev_b32_e32 v43, 2, v43
	v_cndmask_b32_e32 v61, 0, v62, vcc
	v_add_u32_e32 v43, v43, v61
	ds_add_rtn_u32 v45, v43, v9 offset:18688
	v_cmp_lt_i32_e32 vcc, 2, v24
	s_mov_b64 exec, vcc
	s_cbranch_execz .Lk2f_atd
	v_and_b32_e32 v60, 0x1ffff, v28
	v_cmp_le_u32_e32 vcc, s43, v60
	v_ashrrev_i32_e32 v42, 17, v28
	v_lshlrev_b32_e32 v42, 2, v42
	v_cndmask_b32_e32 v61, 0, v62, vcc
	v_add_u32_e32 v42, v42, v61
	ds_add_rtn_u32 v46, v42, v9 offset:18688
	v_cmp_lt_i32_e32 vcc, 3, v24
	s_mov_b64 exec, vcc
	s_cbranch_execz .Lk2f_atd
	v_and_b32_e32 v60, 0x1ffff, v29
	v_cmp_le_u32_e32 vcc, s43, v60
	v_ashrrev_i32_e32 v43, 17, v29
	v_lshlrev_b32_e32 v43, 2, v43
	v_cndmask_b32_e32 v61, 0, v62, vcc
	v_add_u32_e32 v43, v43, v61
	ds_add_rtn_u32 v47, v43, v9 offset:18688
	v_cmp_lt_i32_e32 vcc, 4, v24
	s_mov_b64 exec, vcc
	s_cbranch_execz .Lk2f_atd
	v_and_b32_e32 v60, 0x1ffff, v30
	v_cmp_le_u32_e32 vcc, s43, v60
	v_ashrrev_i32_e32 v42, 17, v30
	v_lshlrev_b32_e32 v42, 2, v42
	v_cndmask_b32_e32 v61, 0, v62, vcc
	v_add_u32_e32 v42, v42, v61
	ds_add_rtn_u32 v48, v42, v9 offset:18688
	v_cmp_lt_i32_e32 vcc, 5, v24
	s_mov_b64 exec, vcc
	s_cbranch_execz .Lk2f_atd
	v_and_b32_e32 v60, 0x1ffff, v31
	v_cmp_le_u32_e32 vcc, s43, v60
	v_ashrrev_i32_e32 v43, 17, v31
	v_lshlrev_b32_e32 v43, 2, v43
	v_cndmask_b32_e32 v61, 0, v62, vcc
	v_add_u32_e32 v43, v43, v61
	ds_add_rtn_u32 v49, v43, v9 offset:18688
	v_cmp_lt_i32_e32 vcc, 6, v24
	s_mov_b64 exec, vcc
	s_cbranch_execz .Lk2f_atd
	v_and_b32_e32 v60, 0x1ffff, v32
	v_cmp_le_u32_e32 vcc, s43, v60
	v_ashrrev_i32_e32 v42, 17, v32
	v_lshlrev_b32_e32 v42, 2, v42
	v_cndmask_b32_e32 v61, 0, v62, vcc
	v_add_u32_e32 v42, v42, v61
	ds_add_rtn_u32 v50, v42, v9 offset:18688
	v_cmp_lt_i32_e32 vcc, 7, v24
	s_mov_b64 exec, vcc
	s_cbranch_execz .Lk2f_atd
	v_and_b32_e32 v60, 0x1ffff, v33
	v_cmp_le_u32_e32 vcc, s43, v60
	v_ashrrev_i32_e32 v43, 17, v33
	v_lshlrev_b32_e32 v43, 2, v43
	v_cndmask_b32_e32 v61, 0, v62, vcc
	v_add_u32_e32 v43, v43, v61
	ds_add_rtn_u32 v51, v43, v9 offset:18688
	v_cmp_lt_i32_e32 vcc, 8, v24
	s_mov_b64 exec, vcc
	s_cbranch_execz .Lk2f_atd
	v_and_b32_e32 v60, 0x1ffff, v34
	v_cmp_le_u32_e32 vcc, s43, v60
	v_ashrrev_i32_e32 v42, 17, v34
	v_lshlrev_b32_e32 v42, 2, v42
	v_cndmask_b32_e32 v61, 0, v62, vcc
	v_add_u32_e32 v42, v42, v61
	ds_add_rtn_u32 v52, v42, v9 offset:18688
	v_cmp_lt_i32_e32 vcc, 9, v24
	s_mov_b64 exec, vcc
	s_cbranch_execz .Lk2f_atd
	v_and_b32_e32 v60, 0x1ffff, v35
	v_cmp_le_u32_e32 vcc, s43, v60
	v_ashrrev_i32_e32 v43, 17, v35
	v_lshlrev_b32_e32 v43, 2, v43
	v_cndmask_b32_e32 v61, 0, v62, vcc
	v_add_u32_e32 v43, v43, v61
	ds_add_rtn_u32 v53, v43, v9 offset:18688
	v_cmp_lt_i32_e32 vcc, 10, v24
	s_mov_b64 exec, vcc
	s_cbranch_execz .Lk2f_atd
	v_and_b32_e32 v60, 0x1ffff, v36
	v_cmp_le_u32_e32 vcc, s43, v60
	v_ashrrev_i32_e32 v42, 17, v36
	v_lshlrev_b32_e32 v42, 2, v42
	v_cndmask_b32_e32 v61, 0, v62, vcc
	v_add_u32_e32 v42, v42, v61
	ds_add_rtn_u32 v54, v42, v9 offset:18688
	v_cmp_lt_i32_e32 vcc, 11, v24
	s_mov_b64 exec, vcc
	s_cbranch_execz .Lk2f_atd
	v_and_b32_e32 v60, 0x1ffff, v37
	v_cmp_le_u32_e32 vcc, s43, v60
	v_ashrrev_i32_e32 v43, 17, v37
	v_lshlrev_b32_e32 v43, 2, v43
	v_cndmask_b32_e32 v61, 0, v62, vcc
	v_add_u32_e32 v43, v43, v61
	ds_add_rtn_u32 v55, v43, v9 offset:18688
	v_cmp_lt_i32_e32 vcc, 12, v24
	s_mov_b64 exec, vcc
	s_cbranch_execz .Lk2f_atd
	v_and_b32_e32 v60, 0x1ffff, v38
	v_cmp_le_u32_e32 vcc, s43, v60
	v_ashrrev_i32_e32 v42, 17, v38
	v_lshlrev_b32_e32 v42, 2, v42
	v_cndmask_b32_e32 v61, 0, v62, vcc
	v_add_u32_e32 v42, v42, v61
	ds_add_rtn_u32 v56, v42, v9 offset:18688
	v_cmp_lt_i32_e32 vcc, 13, v24
	s_mov_b64 exec, vcc
	s_cbranch_execz .Lk2f_atd
	v_and_b32_e32 v60, 0x1ffff, v39
	v_cmp_le_u32_e32 vcc, s43, v60
	v_ashrrev_i32_e32 v43, 17, v39
	v_lshlrev_b32_e32 v43, 2, v43
	v_cndmask_b32_e32 v61, 0, v62, vcc
	v_add_u32_e32 v43, v43, v61
	ds_add_rtn_u32 v57, v43, v9 offset:18688
	v_cmp_lt_i32_e32 vcc, 14, v24
	s_mov_b64 exec, vcc
	s_cbranch_execz .Lk2f_atd
	v_and_b32_e32 v60, 0x1ffff, v40
	v_cmp_le_u32_e32 vcc, s43, v60
	v_ashrrev_i32_e32 v42, 17, v40
	v_lshlrev_b32_e32 v42, 2, v42
	v_cndmask_b32_e32 v61, 0, v62, vcc
	v_add_u32_e32 v42, v42, v61
	ds_add_rtn_u32 v58, v42, v9 offset:18688
	v_cmp_lt_i32_e32 vcc, 15, v24
	s_mov_b64 exec, vcc
	s_cbranch_execz .Lk2f_atd
	v_and_b32_e32 v60, 0x1ffff, v41
	v_cmp_le_u32_e32 vcc, s43, v60
	v_ashrrev_i32_e32 v43, 17, v41
	v_lshlrev_b32_e32 v43, 2, v43
	v_cndmask_b32_e32 v61, 0, v62, vcc
	v_add_u32_e32 v43, v43, v61
	ds_add_rtn_u32 v59, v43, v9 offset:18688
.Lk2f_atd:
	s_mov_b64 exec, -1
	s_waitcnt lgkmcnt(0)
	v_cmp_lt_i32_e32 vcc, 0, v24
	s_mov_b64 exec, vcc
	s_cbranch_execz .Lk2f_sld
	v_and_b32_e32 v43, 0x1ffff, v26
	v_cmp_le_u32_e32 vcc, s43, v43
	v_ashrrev_i32_e32 v42, 17, v26
	v_min_u32_e32 v44, 31, v44
	v_sub_u32_e32 v60, 31, v44
	v_mul_u32_u24_e32 v42, 0x90, v42
	v_cndmask_b32_e32 v60, v44, v60, vcc
	v_lshl_add_u32 v42, v60, 2, v42
	ds_write_b32 v42, v43 offset:19456
	v_cmp_lt_i32_e32 vcc, 1, v24
	s_mov_b64 exec, vcc
	s_cbranch_execz .Lk2f_sld
	v_and_b32_e32 v43, 0x1ffff, v27
	v_cmp_le_u32_e32 vcc, s43, v43
	v_ashrrev_i32_e32 v42, 17, v27
	v_min_u32_e32 v45, 31, v45
	v_sub_u32_e32 v60, 31, v45
	v_mul_u32_u24_e32 v42, 0x90, v42
	v_cndmask_b32_e32 v60, v45, v60, vcc
	v_lshl_add_u32 v42, v60, 2, v42
	ds_write_b32 v42, v43 offset:19456
	v_cmp_lt_i32_e32 vcc, 2, v24
	s_mov_b64 exec, vcc
	s_cbranch_execz .Lk2f_sld
	v_and_b32_e32 v43, 0x1ffff, v28
	v_cmp_le_u32_e32 vcc, s43, v43
	v_ashrrev_i32_e32 v42, 17, v28
	v_min_u32_e32 v46, 31, v46
	v_sub_u32_e32 v60, 31, v46
	v_mul_u32_u24_e32 v42, 0x90, v42
	v_cndmask_b32_e32 v60, v46, v60, vcc
	v_lshl_add_u32 v42, v60, 2, v42
	ds_write_b32 v42, v43 offset:19456
	v_cmp_lt_i32_e32 vcc, 3, v24
	s_mov_b64 exec, vcc
	s_cbranch_execz .Lk2f_sld
	v_and_b32_e32 v43, 0x1ffff, v29
	v_cmp_le_u32_e32 vcc, s43, v43
	v_ashrrev_i32_e32 v42, 17, v29
	v_min_u32_e32 v47, 31, v47
	v_sub_u32_e32 v60, 31, v47
	v_mul_u32_u24_e32 v42, 0x90, v42
	v_cndmask_b32_e32 v60, v47, v60, vcc
	v_lshl_add_u32 v42, v60, 2, v42
	ds_write_b32 v42, v43 offset:19456
	v_cmp_lt_i32_e32 vcc, 4, v24
	s_mov_b64 exec, vcc
	s_cbranch_execz .Lk2f_sld
	v_and_b32_e32 v43, 0x1ffff, v30
	v_cmp_le_u32_e32 vcc, s43, v43
	v_ashrrev_i32_e32 v42, 17, v30
	v_min_u32_e32 v48, 31, v48
	v_sub_u32_e32 v60, 31, v48
	v_mul_u32_u24_e32 v42, 0x90, v42
	v_cndmask_b32_e32 v60, v48, v60, vcc
	v_lshl_add_u32 v42, v60, 2, v42
	ds_write_b32 v42, v43 offset:19456
	v_cmp_lt_i32_e32 vcc, 5, v24
	s_mov_b64 exec, vcc
	s_cbranch_execz .Lk2f_sld
	v_and_b32_e32 v43, 0x1ffff, v31
	v_cmp_le_u32_e32 vcc, s43, v43
	v_ashrrev_i32_e32 v42, 17, v31
	v_min_u32_e32 v49, 31, v49
	v_sub_u32_e32 v60, 31, v49
	v_mul_u32_u24_e32 v42, 0x90, v42
	v_cndmask_b32_e32 v60, v49, v60, vcc
	v_lshl_add_u32 v42, v60, 2, v42
	ds_write_b32 v42, v43 offset:19456
	v_cmp_lt_i32_e32 vcc, 6, v24
	s_mov_b64 exec, vcc
	s_cbranch_execz .Lk2f_sld
	v_and_b32_e32 v43, 0x1ffff, v32
	v_cmp_le_u32_e32 vcc, s43, v43
	v_ashrrev_i32_e32 v42, 17, v32
	v_min_u32_e32 v50, 31, v50
	v_sub_u32_e32 v60, 31, v50
	v_mul_u32_u24_e32 v42, 0x90, v42
	v_cndmask_b32_e32 v60, v50, v60, vcc
	v_lshl_add_u32 v42, v60, 2, v42
	ds_write_b32 v42, v43 offset:19456
	v_cmp_lt_i32_e32 vcc, 7, v24
	s_mov_b64 exec, vcc
	s_cbranch_execz .Lk2f_sld
	v_and_b32_e32 v43, 0x1ffff, v33
	v_cmp_le_u32_e32 vcc, s43, v43
	v_ashrrev_i32_e32 v42, 17, v33
	v_min_u32_e32 v51, 31, v51
	v_sub_u32_e32 v60, 31, v51
	v_mul_u32_u24_e32 v42, 0x90, v42
	v_cndmask_b32_e32 v60, v51, v60, vcc
	v_lshl_add_u32 v42, v60, 2, v42
	ds_write_b32 v42, v43 offset:19456
	v_cmp_lt_i32_e32 vcc, 8, v24
	s_mov_b64 exec, vcc
	s_cbranch_execz .Lk2f_sld
	v_and_b32_e32 v43, 0x1ffff, v34
	v_cmp_le_u32_e32 vcc, s43, v43
	v_ashrrev_i32_e32 v42, 17, v34
	v_min_u32_e32 v52, 31, v52
	v_sub_u32_e32 v60, 31, v52
	v_mul_u32_u24_e32 v42, 0x90, v42
	v_cndmask_b32_e32 v60, v52, v60, vcc
	v_lshl_add_u32 v42, v60, 2, v42
	ds_write_b32 v42, v43 offset:19456
	v_cmp_lt_i32_e32 vcc, 9, v24
	s_mov_b64 exec, vcc
	s_cbranch_execz .Lk2f_sld
	v_and_b32_e32 v43, 0x1ffff, v35
	v_cmp_le_u32_e32 vcc, s43, v43
	v_ashrrev_i32_e32 v42, 17, v35
	v_min_u32_e32 v53, 31, v53
	v_sub_u32_e32 v60, 31, v53
	v_mul_u32_u24_e32 v42, 0x90, v42
	v_cndmask_b32_e32 v60, v53, v60, vcc
	v_lshl_add_u32 v42, v60, 2, v42
	ds_write_b32 v42, v43 offset:19456
	v_cmp_lt_i32_e32 vcc, 10, v24
	s_mov_b64 exec, vcc
	s_cbranch_execz .Lk2f_sld
	v_and_b32_e32 v43, 0x1ffff, v36
	v_cmp_le_u32_e32 vcc, s43, v43
	v_ashrrev_i32_e32 v42, 17, v36
	v_min_u32_e32 v54, 31, v54
	v_sub_u32_e32 v60, 31, v54
	v_mul_u32_u24_e32 v42, 0x90, v42
	v_cndmask_b32_e32 v60, v54, v60, vcc
	v_lshl_add_u32 v42, v60, 2, v42
	ds_write_b32 v42, v43 offset:19456
	v_cmp_lt_i32_e32 vcc, 11, v24
	s_mov_b64 exec, vcc
	s_cbranch_execz .Lk2f_sld
	v_and_b32_e32 v43, 0x1ffff, v37
	v_cmp_le_u32_e32 vcc, s43, v43
	v_ashrrev_i32_e32 v42, 17, v37
	v_min_u32_e32 v55, 31, v55
	v_sub_u32_e32 v60, 31, v55
	v_mul_u32_u24_e32 v42, 0x90, v42
	v_cndmask_b32_e32 v60, v55, v60, vcc
	v_lshl_add_u32 v42, v60, 2, v42
	ds_write_b32 v42, v43 offset:19456
	v_cmp_lt_i32_e32 vcc, 12, v24
	s_mov_b64 exec, vcc
	s_cbranch_execz .Lk2f_sld
	v_and_b32_e32 v43, 0x1ffff, v38
	v_cmp_le_u32_e32 vcc, s43, v43
	v_ashrrev_i32_e32 v42, 17, v38
	v_min_u32_e32 v56, 31, v56
	v_sub_u32_e32 v60, 31, v56
	v_mul_u32_u24_e32 v42, 0x90, v42
	v_cndmask_b32_e32 v60, v56, v60, vcc
	v_lshl_add_u32 v42, v60, 2, v42
	ds_write_b32 v42, v43 offset:19456
	v_cmp_lt_i32_e32 vcc, 13, v24
	s_mov_b64 exec, vcc
	s_cbranch_execz .Lk2f_sld
	v_and_b32_e32 v43, 0x1ffff, v39
	v_cmp_le_u32_e32 vcc, s43, v43
	v_ashrrev_i32_e32 v42, 17, v39
	v_min_u32_e32 v57, 31, v57
	v_sub_u32_e32 v60, 31, v57
	v_mul_u32_u24_e32 v42, 0x90, v42
	v_cndmask_b32_e32 v60, v57, v60, vcc
	v_lshl_add_u32 v42, v60, 2, v42
	ds_write_b32 v42, v43 offset:19456
	v_cmp_lt_i32_e32 vcc, 14, v24
	s_mov_b64 exec, vcc
	s_cbranch_execz .Lk2f_sld
	v_and_b32_e32 v43, 0x1ffff, v40
	v_cmp_le_u32_e32 vcc, s43, v43
	v_ashrrev_i32_e32 v42, 17, v40
	v_min_u32_e32 v58, 31, v58
	v_sub_u32_e32 v60, 31, v58
	v_mul_u32_u24_e32 v42, 0x90, v42
	v_cndmask_b32_e32 v60, v58, v60, vcc
	v_lshl_add_u32 v42, v60, 2, v42
	ds_write_b32 v42, v43 offset:19456
	v_cmp_lt_i32_e32 vcc, 15, v24
	s_mov_b64 exec, vcc
	s_cbranch_execz .Lk2f_sld
	v_and_b32_e32 v43, 0x1ffff, v41
	v_cmp_le_u32_e32 vcc, s43, v43
	v_ashrrev_i32_e32 v42, 17, v41
	v_min_u32_e32 v59, 31, v59
	v_sub_u32_e32 v60, 31, v59
	v_mul_u32_u24_e32 v42, 0x90, v42
	v_cndmask_b32_e32 v60, v59, v60, vcc
	v_lshl_add_u32 v42, v60, 2, v42
	ds_write_b32 v42, v43 offset:19456

.Lk2f_b2:
	s_waitcnt lgkmcnt(0)
	s_barrier
	v_and_b32_e32 v1, 63, v0
	v_lshlrev_b32_e32 v6, 3, v1
	ds_read_b64 v[14:15], v6 offset:18688
	ds_read_b64 v[16:17], v6 offset:38832
	s_cmp_eq_u32 s4, 7
	s_cbranch_scc1 .Lk2f_w7
	v_lshrrev_b32_e32 v3, 2, v1
	s_mul_i32 s5, s4, 14
	v_add_u32_e32 v6, s5, v3
	v_cmp_gt_u32_e32 vcc, 14, v3
	v_mov_b32_e32 v7, 0x7f
	v_mov_b32_e32 v8, 0x62
	v_and_b32_e32 v9, 3, v1
	v_cndmask_b32_e32 v7, v7, v6, vcc
	v_cndmask_b32_e32 v8, v8, v6, vcc
	v_lshlrev_b32_e32 v7, 2, v7
	v_mul_u32_u24_e32 v2, 0x90, v8
	ds_read_b32 v3, v7 offset:18688
	ds_read_b32 v10, v7 offset:38832
	ds_read_b128 v[4:7], v2 offset:19456
	v_lshlrev_b32_e32 v1, 4, v9
	s_mov_b32 s32, s8
	s_and_b32 s33, s9, 0xffff
	s_mov_b32 s34, 0xc35000
	s_mov_b32 s35, 0x20000
	v_and_b32_e32 v8, 15, v0
	v_add_u32_e32 v9, s5, v8
	s_mul_i32 s6, s3, 0x62
	v_add_u32_e32 v9, s6, v9
	v_cmp_gt_u32_e32 vcc, 14, v8
	s_mov_b32 s7, 0x186a0
	v_cmp_gt_u32_e64 s[38:39], s7, v9
	s_and_b64 vcc, vcc, s[38:39]
	s_mov_b64 s[40:41], vcc
	v_and_b32_e32 v8, 0x30, v0
	v_cndmask_b32_e32 v9, 0, v9, vcc
	v_lshl_or_b32 v8, v9, 7, v8
	buffer_load_dwordx4 v[56:59], v8, s[32:35], 0 offen
	buffer_load_dwordx4 v[60:63], v8, s[32:35], 0 offen offset:64
	v_mov_b32_e32 v40, 0
	v_mov_b32_e32 v41, 0
	v_mov_b32_e32 v42, 0
	v_mov_b32_e32 v43, 0
	v_mov_b32_e32 v44, 0
	v_mov_b32_e32 v45, 0
	v_mov_b32_e32 v46, 0
	v_mov_b32_e32 v47, 0
	v_mov_b32_e32 v48, 0
	v_mov_b32_e32 v49, 0
	v_mov_b32_e32 v50, 0
	v_mov_b32_e32 v51, 0
	v_mov_b32_e32 v52, 0
	v_mov_b32_e32 v53, 0
	v_mov_b32_e32 v54, 0
	v_mov_b32_e32 v55, 0
	s_mov_b32 s5, 0
	s_mov_b32 s43, 0x7fffff80
	s_waitcnt lgkmcnt(0)
	v_add_u32_e32 v8, v14, v16
	v_add_u32_e32 v9, v15, v17
	v_max_u32_e32 v8, v8, v9
	v_cmp_lt_u32_e32 vcc, 32, v8
	s_cmp_lg_u64 vcc, 0
	s_cbranch_scc1 .Lk2f_fallback
	v_cmp_lt_i32_e32 vcc, 0, v3
	v_lshl_or_b32 v3, v10, 8, v3
	s_cmp_lg_u64 vcc, 0
	s_cbranch_scc0 .Lk2f_fdone
.Lk2f_loopF:
	v_and_b32_e32 v8, 0xff, v3
	v_subrev_u32_e32 v8, s5, v8
	v_lshl_or_b32 v4, v4, 7, v1
	v_lshl_or_b32 v5, v5, 7, v1
	v_lshl_or_b32 v6, v6, 7, v1
	v_lshl_or_b32 v7, v7, 7, v1
	v_cmp_lt_i32_e64 s[44:45], 0, v8
	v_cmp_lt_i32_e64 s[46:47], 1, v8
	v_cmp_lt_i32_e64 s[48:49], 2, v8
	v_cmp_lt_i32_e64 s[50:51], 3, v8
	v_cmp_lt_i32_e64 s[38:39], 4, v8
	v_mov_b32_e32 v9, s43
	v_cndmask_b32_e64 v4, v9, v4, s[44:45]
	v_cndmask_b32_e64 v5, v9, v5, s[46:47]
	v_cndmask_b32_e64 v6, v9, v6, s[48:49]
	v_cndmask_b32_e64 v7, v9, v7, s[50:51]
	buffer_load_dwordx4 v[8:11], v4, s[32:35], 0 offen
	buffer_load_dwordx4 v[12:15], v4, s[32:35], 0 offen offset:64
	buffer_load_dwordx4 v[16:19], v5, s[32:35], 0 offen
	buffer_load_dwordx4 v[20:23], v5, s[32:35], 0 offen offset:64
	buffer_load_dwordx4 v[24:27], v6, s[32:35], 0 offen
	buffer_load_dwordx4 v[28:31], v6, s[32:35], 0 offen offset:64
	buffer_load_dwordx4 v[32:35], v7, s[32:35], 0 offen
	buffer_load_dwordx4 v[36:39], v7, s[32:35], 0 offen offset:64
	v_add_u32_e32 v2, 16, v2
	s_add_i32 s5, s5, 4
	ds_read_b128 v[4:7], v2 offset:19456
	s_waitcnt vmcnt(5)
	v_pk_add_f16 v8, v8, v16
	v_pk_add_f16 v9, v9, v17
	v_pk_add_f16 v10, v10, v18
	v_pk_add_f16 v11, v11, v19
	s_waitcnt vmcnt(4)
	v_pk_add_f16 v12, v12, v20
	v_pk_add_f16 v13, v13, v21
	v_pk_add_f16 v14, v14, v22
	v_pk_add_f16 v15, v15, v23
	s_waitcnt vmcnt(1)
	v_pk_add_f16 v24, v24, v32
	v_pk_add_f16 v25, v25, v33
	v_pk_add_f16 v26, v26, v34
	v_pk_add_f16 v27, v27, v35
	v_pk_add_f16 v8, v8, v24
	v_pk_add_f16 v9, v9, v25
	v_pk_add_f16 v10, v10, v26
	v_pk_add_f16 v11, v11, v27
	s_waitcnt vmcnt(0)
	v_pk_add_f16 v28, v28, v36
	v_pk_add_f16 v29, v29, v37
	v_pk_add_f16 v30, v30, v38
	v_pk_add_f16 v31, v31, v39
	v_pk_add_f16 v12, v12, v28
	v_pk_add_f16 v13, v13, v29
	v_pk_add_f16 v14, v14, v30
	v_pk_add_f16 v15, v15, v31
	v_fma_mix_f32 v40, v8, 1.0, v40 op_sel:[0,0,0] op_sel_hi:[1,0,0]
	v_fma_mix_f32 v41, v8, 1.0, v41 op_sel:[1,0,0] op_sel_hi:[1,0,0]
	v_fma_mix_f32 v42, v9, 1.0, v42 op_sel:[0,0,0] op_sel_hi:[1,0,0]
	v_fma_mix_f32 v43, v9, 1.0, v43 op_sel:[1,0,0] op_sel_hi:[1,0,0]
	v_fma_mix_f32 v44, v10, 1.0, v44 op_sel:[0,0,0] op_sel_hi:[1,0,0]
	v_fma_mix_f32 v45, v10, 1.0, v45 op_sel:[1,0,0] op_sel_hi:[1,0,0]
	v_fma_mix_f32 v46, v11, 1.0, v46 op_sel:[0,0,0] op_sel_hi:[1,0,0]
	v_fma_mix_f32 v47, v11, 1.0, v47 op_sel:[1,0,0] op_sel_hi:[1,0,0]
	v_fma_mix_f32 v48, v12, 1.0, v48 op_sel:[0,0,0] op_sel_hi:[1,0,0]
	v_fma_mix_f32 v49, v12, 1.0, v49 op_sel:[1,0,0] op_sel_hi:[1,0,0]
	v_fma_mix_f32 v50, v13, 1.0, v50 op_sel:[0,0,0] op_sel_hi:[1,0,0]
	v_fma_mix_f32 v51, v13, 1.0, v51 op_sel:[1,0,0] op_sel_hi:[1,0,0]
	v_fma_mix_f32 v52, v14, 1.0, v52 op_sel:[0,0,0] op_sel_hi:[1,0,0]
	v_fma_mix_f32 v53, v14, 1.0, v53 op_sel:[1,0,0] op_sel_hi:[1,0,0]
	v_fma_mix_f32 v54, v15, 1.0, v54 op_sel:[0,0,0] op_sel_hi:[1,0,0]
	v_fma_mix_f32 v55, v15, 1.0, v55 op_sel:[1,0,0] op_sel_hi:[1,0,0]
	s_waitcnt lgkmcnt(0)
	s_cmp_lg_u64 s[38:39], 0
	s_cbranch_scc1 .Lk2f_loopF
.Lk2f_fdone:
	s_lshl_b32 s6, s5, 2
	v_subrev_u32_e32 v2, s6, v2
	v_add_u32_e32 v2, 0x70, v2
	s_mov_b32 s5, 0
	v_bfe_u32 v8, v3, 8, 8
	v_cmp_lt_i32_e32 vcc, 0, v8
	s_cmp_lg_u64 vcc, 0
	s_cbranch_scc0 .Lk2f_bdone
	ds_read_b128 v[4:7], v2 offset:19456
	s_waitcnt lgkmcnt(0)
.Lk2f_loopB:
	v_bfe_u32 v8, v3, 8, 8
	v_subrev_u32_e32 v8, s5, v8
	v_lshl_or_b32 v4, v4, 7, v1
	v_lshl_or_b32 v5, v5, 7, v1
	v_lshl_or_b32 v6, v6, 7, v1
	v_lshl_or_b32 v7, v7, 7, v1
	v_cmp_lt_i32_e64 s[44:45], 3, v8
	v_cmp_lt_i32_e64 s[46:47], 2, v8
	v_cmp_lt_i32_e64 s[48:49], 1, v8
	v_cmp_lt_i32_e64 s[50:51], 0, v8
	v_cmp_lt_i32_e64 s[38:39], 4, v8
	v_mov_b32_e32 v9, s43
	v_cndmask_b32_e64 v4, v9, v4, s[44:45]
	v_cndmask_b32_e64 v5, v9, v5, s[46:47]
	v_cndmask_b32_e64 v6, v9, v6, s[48:49]
	v_cndmask_b32_e64 v7, v9, v7, s[50:51]
	buffer_load_dwordx4 v[8:11], v4, s[32:35], 0 offen
	buffer_load_dwordx4 v[12:15], v4, s[32:35], 0 offen offset:64
	buffer_load_dwordx4 v[16:19], v5, s[32:35], 0 offen
	buffer_load_dwordx4 v[20:23], v5, s[32:35], 0 offen offset:64
	buffer_load_dwordx4 v[24:27], v6, s[32:35], 0 offen
	buffer_load_dwordx4 v[28:31], v6, s[32:35], 0 offen offset:64
	buffer_load_dwordx4 v[32:35], v7, s[32:35], 0 offen
	buffer_load_dwordx4 v[36:39], v7, s[32:35], 0 offen offset:64
	v_add_u32_e32 v2, -16, v2
	s_add_i32 s5, s5, 4
	ds_read_b128 v[4:7], v2 offset:19456
	s_waitcnt vmcnt(5)
	v_pk_add_f16 v8, v8, v16
	v_pk_add_f16 v9, v9, v17
	v_pk_add_f16 v10, v10, v18
	v_pk_add_f16 v11, v11, v19
	s_waitcnt vmcnt(4)
	v_pk_add_f16 v12, v12, v20
	v_pk_add_f16 v13, v13, v21
	v_pk_add_f16 v14, v14, v22
	v_pk_add_f16 v15, v15, v23
	s_waitcnt vmcnt(1)
	v_pk_add_f16 v24, v24, v32
	v_pk_add_f16 v25, v25, v33
	v_pk_add_f16 v26, v26, v34
	v_pk_add_f16 v27, v27, v35
	v_pk_add_f16 v8, v8, v24
	v_pk_add_f16 v9, v9, v25
	v_pk_add_f16 v10, v10, v26
	v_pk_add_f16 v11, v11, v27
	s_waitcnt vmcnt(0)
	v_pk_add_f16 v28, v28, v36
	v_pk_add_f16 v29, v29, v37
	v_pk_add_f16 v30, v30, v38
	v_pk_add_f16 v31, v31, v39
	v_pk_add_f16 v12, v12, v28
	v_pk_add_f16 v13, v13, v29
	v_pk_add_f16 v14, v14, v30
	v_pk_add_f16 v15, v15, v31
	v_fma_mix_f32 v40, v8, 1.0, v40 op_sel:[0,0,0] op_sel_hi:[1,0,0]
	v_fma_mix_f32 v41, v8, 1.0, v41 op_sel:[1,0,0] op_sel_hi:[1,0,0]
	v_fma_mix_f32 v42, v9, 1.0, v42 op_sel:[0,0,0] op_sel_hi:[1,0,0]
	v_fma_mix_f32 v43, v9, 1.0, v43 op_sel:[1,0,0] op_sel_hi:[1,0,0]
	v_fma_mix_f32 v44, v10, 1.0, v44 op_sel:[0,0,0] op_sel_hi:[1,0,0]
	v_fma_mix_f32 v45, v10, 1.0, v45 op_sel:[1,0,0] op_sel_hi:[1,0,0]
	v_fma_mix_f32 v46, v11, 1.0, v46 op_sel:[0,0,0] op_sel_hi:[1,0,0]
	v_fma_mix_f32 v47, v11, 1.0, v47 op_sel:[1,0,0] op_sel_hi:[1,0,0]
	v_fma_mix_f32 v48, v12, 1.0, v48 op_sel:[0,0,0] op_sel_hi:[1,0,0]
	v_fma_mix_f32 v49, v12, 1.0, v49 op_sel:[1,0,0] op_sel_hi:[1,0,0]
	v_fma_mix_f32 v50, v13, 1.0, v50 op_sel:[0,0,0] op_sel_hi:[1,0,0]
	v_fma_mix_f32 v51, v13, 1.0, v51 op_sel:[1,0,0] op_sel_hi:[1,0,0]
	v_fma_mix_f32 v52, v14, 1.0, v52 op_sel:[0,0,0] op_sel_hi:[1,0,0]
	v_fma_mix_f32 v53, v14, 1.0, v53 op_sel:[1,0,0] op_sel_hi:[1,0,0]
	v_fma_mix_f32 v54, v15, 1.0, v54 op_sel:[0,0,0] op_sel_hi:[1,0,0]
	v_fma_mix_f32 v55, v15, 1.0, v55 op_sel:[1,0,0] op_sel_hi:[1,0,0]
	s_waitcnt lgkmcnt(0)
	s_cmp_lg_u64 s[38:39], 0
	s_cbranch_scc1 .Lk2f_loopB
.Lk2f_bdone:
	v_bfe_u32 v4, v3, 8, 8
	v_and_b32_e32 v3, 0xff, v3
	v_add_u32_e32 v3, v3, v4

.Lk2f_w7:
	v_mov_b32_e32 v8, 0
	ds_read_b128 v[4:7], v8 offset:19216
	s_waitcnt lgkmcnt(0)
	v_mov_b32_e32 v32, v14
	v_mov_b32_e32 v33, v15
	v_mov_b32_e32 v34, v16
	v_mov_b32_e32 v35, v17
	v_add_u32_e32 v14, v14, v16
	v_add_u32_e32 v15, v15, v17
	v_max_u32_e32 v9, v14, v15
	v_cmp_lt_u32_e32 vcc, 32, v9
	s_cmp_lg_u64 vcc, 0
	s_cbranch_scc1 .Lk2f_fallback
	v_add3_u32 v4, v4, v5, v6
	v_add_u32_e32 v4, v4, v7
	v_add_u32_e32 v11, v14, v15
	s_nop 1
	v_add_u32_dpp v12, v11, v11 row_shr:1 row_mask:0xf bank_mask:0xf bound_ctrl:1
	s_nop 1
	v_add_u32_dpp v12, v12, v12 row_shr:2 row_mask:0xf bank_mask:0xf bound_ctrl:1
	s_nop 1
	v_add_u32_dpp v12, v12, v12 row_shr:4 row_mask:0xf bank_mask:0xf bound_ctrl:1
	s_nop 1
	v_add_u32_dpp v12, v12, v12 row_shr:8 row_mask:0xf bank_mask:0xf bound_ctrl:1
	s_nop 1
	v_add_u32_dpp v12, v12, v12 row_bcast:15 row_mask:0xa bank_mask:0xf
	s_nop 1
	v_add_u32_dpp v12, v12, v12 row_bcast:31 row_mask:0xc bank_mask:0xf
	v_sub_u32_e32 v12, v12, v11
	v_add_u32_e32 v12, v12, v4
	v_add_u32_e32 v13, v12, v14
	s_mul_i32 s6, s3, 0x62
	v_lshl_add_u32 v16, v1, 1, s6
	s_movk_i32 s7, 49
	v_cmp_gt_u32_e32 vcc, s7, v1
	s_mov_b32 s7, 0x186a0
	v_cmp_gt_u32_e64 s[38:39], s7, v16
	s_and_b64 vcc, vcc, s[38:39]
	v_lshlrev_b32_e32 v17, 2, v16
	s_and_saveexec_b64 s[40:41], vcc
	s_cbranch_execz .Lk2f_w7a
	global_store_dwordx2 v17, v[12:13], s[14:15]

.Lk2f_w7b:
	v_sub_u32_e32 v16, v12, v4
	v_sub_u32_e32 v17, v13, v4
	v_add_u32_e32 v20, v17, v15
	v_readfirstlane_b32 s39, v4
	v_readlane_b32 s38, v20, 63
	s_lshl_b32 s39, s39, 2
	s_cmpk_gt_u32 s38, 0x480
	s_cbranch_scc1 .Lk2f_w7slow
	v_min_u32_e32 v18, 48, v1
	v_mul_u32_u24_e32 v18, 0x120, v18
	v_mov_b32_e32 v28, v32
	v_mov_b32_e32 v30, v33
	v_add_u32_e32 v29, -28, v34
	v_add_u32_e32 v31, -28, v35
	v_lshlrev_b32_e32 v36, 2, v16
	v_lshlrev_b32_e32 v38, 2, v17
	v_add3_u32 v37, v16, v32, 28
	v_add3_u32 v39, v17, v33, 28
	v_lshlrev_b32_e32 v37, 2, v37
	v_lshlrev_b32_e32 v39, 2, v39
	s_mov_b32 s5, 0
.Lk2f_cptop:
	ds_read_b128 v[20:23], v18 offset:19456
	ds_read_b128 v[24:27], v18 offset:19600
	s_waitcnt lgkmcnt(0)
	v_cmp_lt_i32_e32 vcc, 0, v28
	s_and_saveexec_b64 s[40:41], vcc
	s_cbranch_execz .Lk2f_cpa0
	ds_write_b32 v36, v20 offset:33712
.Lk2f_cpa0:
	s_mov_b64 exec, s[40:41]
	v_cmp_lt_i32_e32 vcc, 1, v28
	s_and_saveexec_b64 s[40:41], vcc
	s_cbranch_execz .Lk2f_cpa1
	ds_write_b32 v36, v21 offset:33716
.Lk2f_cpa1:
	s_mov_b64 exec, s[40:41]
	v_cmp_lt_i32_e32 vcc, 2, v28
	s_and_saveexec_b64 s[40:41], vcc
	s_cbranch_execz .Lk2f_cpa2
	ds_write_b32 v36, v22 offset:33720
.Lk2f_cpa2:
	s_mov_b64 exec, s[40:41]
	v_cmp_lt_i32_e32 vcc, 3, v28
	s_and_saveexec_b64 s[40:41], vcc
	s_cbranch_execz .Lk2f_cpa3
	ds_write_b32 v36, v23 offset:33724
.Lk2f_cpa3:
	s_mov_b64 exec, s[40:41]
	v_cmp_lt_i32_e32 vcc, 3, v29
	s_and_saveexec_b64 s[40:41], vcc
	s_cbranch_execz .Lk2f_cpb0
	ds_write_b32 v37, v20 offset:33724
.Lk2f_cpb0:
	s_mov_b64 exec, s[40:41]
	v_cmp_lt_i32_e32 vcc, 2, v29
	s_and_saveexec_b64 s[40:41], vcc
	s_cbranch_execz .Lk2f_cpb1
	ds_write_b32 v37, v21 offset:33720
.Lk2f_cpb1:
	s_mov_b64 exec, s[40:41]
	v_cmp_lt_i32_e32 vcc, 1, v29
	s_and_saveexec_b64 s[40:41], vcc
	s_cbranch_execz .Lk2f_cpb2
	ds_write_b32 v37, v22 offset:33716
.Lk2f_cpb2:
	s_mov_b64 exec, s[40:41]
	v_cmp_lt_i32_e32 vcc, 0, v29
	s_and_saveexec_b64 s[40:41], vcc
	s_cbranch_execz .Lk2f_cpb3
	ds_write_b32 v37, v23 offset:33712
.Lk2f_cpb3:
	s_mov_b64 exec, s[40:41]
	v_cmp_lt_i32_e32 vcc, 0, v30
	s_and_saveexec_b64 s[40:41], vcc
	s_cbranch_execz .Lk2f_cpc0
	ds_write_b32 v38, v24 offset:33712
.Lk2f_cpc0:
	s_mov_b64 exec, s[40:41]
	v_cmp_lt_i32_e32 vcc, 1, v30
	s_and_saveexec_b64 s[40:41], vcc
	s_cbranch_execz .Lk2f_cpc1
	ds_write_b32 v38, v25 offset:33716
.Lk2f_cpc1:
	s_mov_b64 exec, s[40:41]
	v_cmp_lt_i32_e32 vcc, 2, v30
	s_and_saveexec_b64 s[40:41], vcc
	s_cbranch_execz .Lk2f_cpc2
	ds_write_b32 v38, v26 offset:33720
.Lk2f_cpc2:
	s_mov_b64 exec, s[40:41]
	v_cmp_lt_i32_e32 vcc, 3, v30
	s_and_saveexec_b64 s[40:41], vcc
	s_cbranch_execz .Lk2f_cpc3
	ds_write_b32 v38, v27 offset:33724
.Lk2f_cpc3:
	s_mov_b64 exec, s[40:41]
	v_cmp_lt_i32_e32 vcc, 3, v31
	s_and_saveexec_b64 s[40:41], vcc
	s_cbranch_execz .Lk2f_cpd0
	ds_write_b32 v39, v24 offset:33724
.Lk2f_cpd0:
	s_mov_b64 exec, s[40:41]
	v_cmp_lt_i32_e32 vcc, 2, v31
	s_and_saveexec_b64 s[40:41], vcc
	s_cbranch_execz .Lk2f_cpd1
	ds_write_b32 v39, v25 offset:33720
.Lk2f_cpd1:
	s_mov_b64 exec, s[40:41]
	v_cmp_lt_i32_e32 vcc, 1, v31
	s_and_saveexec_b64 s[40:41], vcc
	s_cbranch_execz .Lk2f_cpd2
	ds_write_b32 v39, v26 offset:33716
.Lk2f_cpd2:
	s_mov_b64 exec, s[40:41]
	v_cmp_lt_i32_e32 vcc, 0, v31
	s_and_saveexec_b64 s[40:41], vcc
	s_cbranch_execz .Lk2f_cpd3
	ds_write_b32 v39, v27 offset:33712
.Lk2f_cpd3:
	s_mov_b64 exec, s[40:41]
	v_add_u32_e32 v28, -4, v28
	v_add_u32_e32 v30, -4, v30
	v_add_u32_e32 v29, 4, v29
	v_add_u32_e32 v31, 4, v31
	v_add_u32_e32 v36, 16, v36
	v_add_u32_e32 v38, 16, v38
	v_add_u32_e32 v37, -16, v37
	v_add_u32_e32 v39, -16, v39
	v_add_u32_e32 v18, 16, v18
	s_add_i32 s5, s5, 4
	s_cmp_lt_u32 s5, 32
	s_cbranch_scc1 .Lk2f_cptop

.Lk2f_w7slow:
	v_min_u32_e32 v18, 48, v1
	v_mul_u32_u24_e32 v18, 0x120, v18
	v_mov_b32_e32 v28, v32
	v_mov_b32_e32 v30, v33
	v_add_u32_e32 v29, -28, v34
	v_add_u32_e32 v31, -28, v35
	v_lshlrev_b32_e32 v36, 2, v12
	v_lshlrev_b32_e32 v38, 2, v13
	v_add3_u32 v37, v12, v32, 28
	v_add3_u32 v39, v13, v33, 28
	v_lshlrev_b32_e32 v37, 2, v37
	v_lshlrev_b32_e32 v39, 2, v39
	s_mov_b32 s5, 0
.Lk2f_cgtop:
	ds_read_b128 v[20:23], v18 offset:19456
	ds_read_b128 v[24:27], v18 offset:19600
	s_waitcnt lgkmcnt(0)
	v_cmp_lt_i32_e32 vcc, 0, v28
	s_and_saveexec_b64 s[40:41], vcc
	s_cbranch_execz .Lk2f_cga0
	global_store_dword v36, v20, s[16:17] offset:0
.Lk2f_cga0:
	s_mov_b64 exec, s[40:41]
	v_cmp_lt_i32_e32 vcc, 1, v28
	s_and_saveexec_b64 s[40:41], vcc
	s_cbranch_execz .Lk2f_cga1
	global_store_dword v36, v21, s[16:17] offset:4
.Lk2f_cga1:
	s_mov_b64 exec, s[40:41]
	v_cmp_lt_i32_e32 vcc, 2, v28
	s_and_saveexec_b64 s[40:41], vcc
	s_cbranch_execz .Lk2f_cga2
	global_store_dword v36, v22, s[16:17] offset:8
.Lk2f_cga2:
	s_mov_b64 exec, s[40:41]
	v_cmp_lt_i32_e32 vcc, 3, v28
	s_and_saveexec_b64 s[40:41], vcc
	s_cbranch_execz .Lk2f_cga3
	global_store_dword v36, v23, s[16:17] offset:12
.Lk2f_cga3:
	s_mov_b64 exec, s[40:41]
	v_cmp_lt_i32_e32 vcc, 3, v29
	s_and_saveexec_b64 s[40:41], vcc
	s_cbranch_execz .Lk2f_cgb0
	global_store_dword v37, v20, s[16:17] offset:12
.Lk2f_cgb0:
	s_mov_b64 exec, s[40:41]
	v_cmp_lt_i32_e32 vcc, 2, v29
	s_and_saveexec_b64 s[40:41], vcc
	s_cbranch_execz .Lk2f_cgb1
	global_store_dword v37, v21, s[16:17] offset:8
.Lk2f_cgb1:
	s_mov_b64 exec, s[40:41]
	v_cmp_lt_i32_e32 vcc, 1, v29
	s_and_saveexec_b64 s[40:41], vcc
	s_cbranch_execz .Lk2f_cgb2
	global_store_dword v37, v22, s[16:17] offset:4
.Lk2f_cgb2:
	s_mov_b64 exec, s[40:41]
	v_cmp_lt_i32_e32 vcc, 0, v29
	s_and_saveexec_b64 s[40:41], vcc
	s_cbranch_execz .Lk2f_cgb3
	global_store_dword v37, v23, s[16:17] offset:0
.Lk2f_cgb3:
	s_mov_b64 exec, s[40:41]
	v_cmp_lt_i32_e32 vcc, 0, v30
	s_and_saveexec_b64 s[40:41], vcc
	s_cbranch_execz .Lk2f_cgc0
	global_store_dword v38, v24, s[16:17] offset:0
.Lk2f_cgc0:
	s_mov_b64 exec, s[40:41]
	v_cmp_lt_i32_e32 vcc, 1, v30
	s_and_saveexec_b64 s[40:41], vcc
	s_cbranch_execz .Lk2f_cgc1
	global_store_dword v38, v25, s[16:17] offset:4
.Lk2f_cgc1:
	s_mov_b64 exec, s[40:41]
	v_cmp_lt_i32_e32 vcc, 2, v30
	s_and_saveexec_b64 s[40:41], vcc
	s_cbranch_execz .Lk2f_cgc2
	global_store_dword v38, v26, s[16:17] offset:8
.Lk2f_cgc2:
	s_mov_b64 exec, s[40:41]
	v_cmp_lt_i32_e32 vcc, 3, v30
	s_and_saveexec_b64 s[40:41], vcc
	s_cbranch_execz .Lk2f_cgc3
	global_store_dword v38, v27, s[16:17] offset:12
.Lk2f_cgc3:
	s_mov_b64 exec, s[40:41]
	v_cmp_lt_i32_e32 vcc, 3, v31
	s_and_saveexec_b64 s[40:41], vcc
	s_cbranch_execz .Lk2f_cgd0
	global_store_dword v39, v24, s[16:17] offset:12
.Lk2f_cgd0:
	s_mov_b64 exec, s[40:41]
	v_cmp_lt_i32_e32 vcc, 2, v31
	s_and_saveexec_b64 s[40:41], vcc
	s_cbranch_execz .Lk2f_cgd1
	global_store_dword v39, v25, s[16:17] offset:8
.Lk2f_cgd1:
	s_mov_b64 exec, s[40:41]
	v_cmp_lt_i32_e32 vcc, 1, v31
	s_and_saveexec_b64 s[40:41], vcc
	s_cbranch_execz .Lk2f_cgd2
	global_store_dword v39, v26, s[16:17] offset:4
.Lk2f_cgd2:
	s_mov_b64 exec, s[40:41]
	v_cmp_lt_i32_e32 vcc, 0, v31
	s_and_saveexec_b64 s[40:41], vcc
	s_cbranch_execz .Lk2f_cgd3
	global_store_dword v39, v27, s[16:17] offset:0
.Lk2f_cgd3:
	s_mov_b64 exec, s[40:41]
	v_add_u32_e32 v28, -4, v28
	v_add_u32_e32 v30, -4, v30
	v_add_u32_e32 v29, 4, v29
	v_add_u32_e32 v31, 4, v31
	v_add_u32_e32 v36, 16, v36
	v_add_u32_e32 v38, 16, v38
	v_add_u32_e32 v37, -16, v37
	v_add_u32_e32 v39, -16, v39
	v_add_u32_e32 v18, 16, v18
	s_add_i32 s5, s5, 4
	s_cmp_lt_u32 s5, 32
	s_cbranch_scc1 .Lk2f_cgtop
	s_endpgm

	.amdhsa_kernel _Z8k_layer1PKDF16_PKiS2_PiS3_PKDv4_jS6_PKfS8_P15HIP_vector_typeIfLj2EESB_
		.amdhsa_group_segment_fixed_size 39344
		.amdhsa_private_segment_fixed_size 0
		.amdhsa_kernarg_size 88
		.amdhsa_user_sgpr_count 2
		.amdhsa_user_sgpr_dispatch_ptr 0
		.amdhsa_user_sgpr_queue_ptr 0
		.amdhsa_user_sgpr_kernarg_segment_ptr 1
		.amdhsa_user_sgpr_dispatch_id 0
		.amdhsa_user_sgpr_kernarg_preload_length 0
		.amdhsa_user_sgpr_kernarg_preload_offset 0
		.amdhsa_user_sgpr_private_segment_size 0
		.amdhsa_uses_dynamic_stack 0
		.amdhsa_enable_private_segment 0
		.amdhsa_system_sgpr_workgroup_id_x 1
		.amdhsa_system_sgpr_workgroup_id_y 0
		.amdhsa_system_sgpr_workgroup_id_z 0
		.amdhsa_system_sgpr_workgroup_info 0
		.amdhsa_system_vgpr_workitem_id 0
		.amdhsa_next_free_vgpr 64
		.amdhsa_next_free_sgpr 70
		.amdhsa_accum_offset 64
		.amdhsa_reserve_vcc 1
		.amdhsa_float_round_mode_32 0
		.amdhsa_float_round_mode_16_64 0
		.amdhsa_float_denorm_mode_32 3
		.amdhsa_float_denorm_mode_16_64 3
		.amdhsa_dx10_clamp 1
		.amdhsa_ieee_mode 1
		.amdhsa_fp16_overflow 0
		.amdhsa_tg_split 0
		.amdhsa_exception_fp_ieee_invalid_op 0
		.amdhsa_exception_fp_denorm_src 0
		.amdhsa_exception_fp_ieee_div_zero 0
		.amdhsa_exception_fp_ieee_overflow 0
		.amdhsa_exception_fp_ieee_underflow 0
		.amdhsa_exception_fp_ieee_inexact 0
		.amdhsa_exception_int_div_zero 0
	.end_amdhsa_kernel

amdhsa.kernels:
  - .agpr_count:     0
    .args:
      - .actual_access:  read_only
        .address_space:  global
        .offset:         0
        .size:           8
        .value_kind:     global_buffer
      - .actual_access:  read_only
        .address_space:  global
        .offset:         8
        .size:           8
        .value_kind:     global_buffer
      - .actual_access:  read_only
        .address_space:  global
        .offset:         16
        .size:           8
        .value_kind:     global_buffer
      - .actual_access:  read_only
        .address_space:  global
        .offset:         24
        .size:           8
        .value_kind:     global_buffer
      - .actual_access:  read_only
        .address_space:  global
        .offset:         32
        .size:           8
        .value_kind:     global_buffer
      - .actual_access:  read_only
        .address_space:  global
        .offset:         40
        .size:           8
        .value_kind:     global_buffer
      - .actual_access:  write_only
        .address_space:  global
        .offset:         48
        .size:           8
        .value_kind:     global_buffer
      - .actual_access:  write_only
        .address_space:  global
        .offset:         56
        .size:           8
        .value_kind:     global_buffer
      - .actual_access:  write_only
        .address_space:  global
        .offset:         64
        .size:           8
        .value_kind:     global_buffer
      - .actual_access:  write_only
        .address_space:  global
        .offset:         72
        .size:           8
        .value_kind:     global_buffer
      - .actual_access:  write_only
        .address_space:  global
        .offset:         80
        .size:           8
        .value_kind:     global_buffer
    .group_segment_fixed_size: 20544
    .kernarg_segment_align: 8
    .kernarg_segment_size: 88
    .language:       OpenCL C
    .language_version:
      - 2
      - 0
    .max_flat_workgroup_size: 1024
    .name:           _Z6k_partPKiPKfS2_S2_S2_S2_PiS3_PDF16_S4_S4_
    .private_segment_fixed_size: 0
    .sgpr_count:     28
    .sgpr_spill_count: 0
    .symbol:         _Z6k_partPKiPKfS2_S2_S2_S2_PiS3_PDF16_S4_S4_.kd
    .uniform_work_group_size: 1
    .uses_dynamic_stack: false
    .vgpr_count:     44
    .vgpr_spill_count: 0
    .wavefront_size: 64
  - .agpr_count:     0
    .args:
      - .actual_access:  read_only
        .address_space:  global
        .offset:         0
        .size:           8
        .value_kind:     global_buffer
      - .actual_access:  read_only
        .address_space:  global
        .offset:         8
        .size:           8
        .value_kind:     global_buffer
      - .actual_access:  read_only
        .address_space:  global
        .offset:         16
        .size:           8
        .value_kind:     global_buffer
      - .actual_access:  write_only
        .address_space:  global
        .offset:         24
        .size:           8
        .value_kind:     global_buffer
      - .address_space:  global
        .offset:         32
        .size:           8
        .value_kind:     global_buffer
      - .actual_access:  read_only
        .address_space:  global
        .offset:         40
        .size:           8
        .value_kind:     global_buffer
      - .actual_access:  read_only
        .address_space:  global
        .offset:         48
        .size:           8
        .value_kind:     global_buffer
      - .actual_access:  read_only
        .address_space:  global
        .offset:         56
        .size:           8
        .value_kind:     global_buffer
      - .actual_access:  read_only
        .address_space:  global
        .offset:         64
        .size:           8
        .value_kind:     global_buffer
      - .actual_access:  write_only
        .address_space:  global
        .offset:         72
        .size:           8
        .value_kind:     global_buffer
      - .actual_access:  write_only
        .address_space:  global
        .offset:         80
        .size:           8
        .value_kind:     global_buffer
    .group_segment_fixed_size: 39344
    .kernarg_segment_align: 8
    .kernarg_segment_size: 88
    .language:       OpenCL C
    .language_version:
      - 2
      - 0
    .max_flat_workgroup_size: 512
    .name:           _Z8k_layer1PKDF16_PKiS2_PiS3_PKDv4_jS6_PKfS8_P15HIP_vector_typeIfLj2EESB_
    .private_segment_fixed_size: 0
    .sgpr_count:     76
    .sgpr_spill_count: 0
    .symbol:         _Z8k_layer1PKDF16_PKiS2_PiS3_PKDv4_jS6_PKfS8_P15HIP_vector_typeIfLj2EESB_.kd
    .uniform_work_group_size: 1
    .uses_dynamic_stack: false
    .vgpr_count:     64
    .vgpr_spill_count: 0
    .wavefront_size: 64
  - .agpr_count:     0
    .args:
      - .actual_access:  read_only
        .address_space:  global
        .offset:         0
        .size:           8
        .value_kind:     global_buffer
      - .actual_access:  read_only
        .address_space:  global
        .offset:         8
        .size:           8
        .value_kind:     global_buffer
      - .actual_access:  read_only
        .address_space:  global
        .offset:         16
        .size:           8
        .value_kind:     global_buffer
      - .actual_access:  read_only
        .address_space:  global
        .offset:         24
        .size:           8
        .value_kind:     global_buffer
      - .actual_access:  write_only
        .address_space:  global
        .offset:         32
        .size:           8
        .value_kind:     global_buffer
    .group_segment_fixed_size: 0
    .kernarg_segment_align: 8
    .kernarg_segment_size: 40
    .language:       OpenCL C
    .language_version:
      - 2
      - 0
    .max_flat_workgroup_size: 448
    .name:           _Z8k_layer2PK15HIP_vector_typeIfLj2EES2_PKiS4_PS0_
    .private_segment_fixed_size: 0
    .sgpr_count:     21
    .sgpr_spill_count: 0
    .symbol:         _Z8k_layer2PK15HIP_vector_typeIfLj2EES2_PKiS4_PS0_.kd
    .uniform_work_group_size: 1
    .uses_dynamic_stack: false
    .vgpr_count:     25
    .vgpr_spill_count: 0
    .wavefront_size: 64
